# baseline (speedup 1.0000x reference)
amdhsa.kernels:
  - .agpr_count:     0
    .args:
      - .actual_access:  read_only
        .address_space:  global
        .offset:         0
        .size:           8
        .value_kind:     global_buffer
      - .actual_access:  read_only
        .address_space:  global
        .offset:         8
        .size:           8
        .value_kind:     global_buffer
      - .actual_access:  read_only
        .address_space:  global
        .offset:         16
        .size:           8
        .value_kind:     global_buffer
      - .actual_access:  read_only
        .address_space:  global
        .offset:         24
        .size:           8
        .value_kind:     global_buffer
      - .actual_access:  write_only
        .address_space:  global
        .offset:         32
        .size:           8
        .value_kind:     global_buffer
    .group_segment_fixed_size: 0
    .kernarg_segment_align: 8
    .kernarg_segment_size: 40
    .language:       OpenCL C
    .language_version:
      - 2
      - 0
    .max_flat_workgroup_size: 256
    .name:           _Z11prep_kernelPKfS0_S0_S0_Pc
    .private_segment_fixed_size: 0
    .sgpr_count:     30
    .sgpr_spill_count: 0
    .symbol:         _Z11prep_kernelPKfS0_S0_S0_Pc.kd
    .uniform_work_group_size: 1
    .uses_dynamic_stack: false
    .vgpr_count:     20
    .vgpr_spill_count: 0
    .wavefront_size: 64
  - .agpr_count:     0
    .args:
      - .address_space:  global
        .offset:         0
        .size:           8
        .value_kind:     global_buffer
      - .actual_access:  read_only
        .address_space:  global
        .offset:         8
        .size:           8
        .value_kind:     global_buffer
      - .actual_access:  read_only
        .address_space:  global
        .offset:         16
        .size:           8
        .value_kind:     global_buffer
      - .address_space:  global
        .offset:         24
        .size:           8
        .value_kind:     global_buffer
      - .actual_access:  write_only
        .address_space:  global
        .offset:         32
        .size:           8
        .value_kind:     global_buffer
      - .address_space:  global
        .offset:         40
        .size:           8
        .value_kind:     global_buffer
    .group_segment_fixed_size: 133120
    .kernarg_segment_align: 8
    .kernarg_segment_size: 48
    .language:       OpenCL C
    .language_version:
      - 2
      - 0
    .max_flat_workgroup_size: 512
    .name:           _Z13router_kernelPKfS0_S0_PcPfS1_
    .private_segment_fixed_size: 0
    .sgpr_count:     106
    .sgpr_spill_count: 7
    .symbol:         _Z13router_kernelPKfS0_S0_PcPfS1_.kd
    .uniform_work_group_size: 1
    .uses_dynamic_stack: false
    .vgpr_count:     239
    .vgpr_spill_count: 0
    .wavefront_size: 64
  - .agpr_count:     0
    .args:
      - .address_space:  global
        .offset:         0
        .size:           8
        .value_kind:     global_buffer
    .group_segment_fixed_size: 20
    .kernarg_segment_align: 8
    .kernarg_segment_size: 8
    .language:       OpenCL C
    .language_version:
      - 2
      - 0
    .max_flat_workgroup_size: 320
    .name:           _Z11plan_kernelPc
    .private_segment_fixed_size: 0
    .sgpr_count:     16
    .sgpr_spill_count: 0
    .symbol:         _Z11plan_kernelPc.kd
    .uniform_work_group_size: 1
    .uses_dynamic_stack: false
    .vgpr_count:     20
    .vgpr_spill_count: 0
    .wavefront_size: 64
  - .agpr_count:     96
    .args:
      - .actual_access:  read_only
        .address_space:  global
        .offset:         0
        .size:           8
        .value_kind:     global_buffer
      - .actual_access:  read_only
        .address_space:  global
        .offset:         8
        .size:           8
        .value_kind:     global_buffer
      - .address_space:  global
        .offset:         16
        .size:           8
        .value_kind:     global_buffer
      - .actual_access:  write_only
        .address_space:  global
        .offset:         24
        .size:           8
        .value_kind:     global_buffer
    .group_segment_fixed_size: 78784
    .kernarg_segment_align: 8
    .kernarg_segment_size: 32
    .language:       OpenCL C
    .language_version:
      - 2
      - 0
    .max_flat_workgroup_size: 256
    .name:           _Z13expert_kernelPKfS0_PKcPf
    .private_segment_fixed_size: 0
    .sgpr_count:     58
    .sgpr_spill_count: 0
    .symbol:         _Z13expert_kernelPKfS0_PKcPf.kd
    .uniform_work_group_size: 1
    .uses_dynamic_stack: false
    .vgpr_count:     256
    .vgpr_spill_count: 0
    .wavefront_size: 64
